# P9: residual tile lines touched from inside the K-loop (iterations 2..5, one discarded 4-byte load per lane) so the epilogue's residual loads hit the caches while HBM was idle
# speedup vs baseline: 1.0045x; 1.0045x over previous
.LBB0_1182:
	ds_read_b128 v[146:149], v225
	ds_read_b128 v[150:153], v225 offset:1024
	ds_read_b128 v[154:157], v225 offset:2048
	ds_read_b128 v[158:161], v225 offset:3072
	ds_read_b128 v[106:109], v226
	ds_read_b128 v[110:113], v226 offset:1024
	ds_read_b128 v[122:125], v226 offset:2048
	ds_read_b128 v[126:129], v226 offset:3072
	s_cmp_eq_u32 s34, 0
	s_cselect_b64 s[36:37], -1, 0
	v_lshl_add_u64 v[216:217], v[212:213], 0, s[34:35]
	s_add_i32 m0, s27, 0xc000
	ds_read_b128 v[186:189], v227
	ds_read_b128 v[190:193], v227 offset:1024
	ds_read_b128 v[178:181], v227 offset:2048
	ds_read_b128 v[182:185], v227 offset:3072
	ds_read_b128 v[170:173], v227 offset:4096
	ds_read_b128 v[174:177], v227 offset:5120
	ds_read_b128 v[162:165], v227 offset:6144
	ds_read_b128 v[166:169], v227 offset:7168
	global_load_lds_dwordx4 v[216:217], off
	v_lshl_add_u64 v[216:217], v[214:215], 0, s[34:35]
	s_add_i32 m0, s27, 0xe000
	s_and_b64 s[36:37], s[30:31], s[36:37]
	global_load_lds_dwordx4 v[216:217], off
	s_lshr_b32 s66, s34, 8
	s_sub_u32 s66, s66, 2
	s_cmp_gt_u32 s66, 3
	s_cbranch_scc1 .Ltch9_skip
	s_and_b32 s67, s66, 1
	s_lshl_b32 s67, s67, 19
	s_lshr_b32 s66, s66, 1
	s_lshl_b32 s66, s66, 21
	s_add_u32 s66, s66, s67
	v_and_b32_e32 v246, 63, v0
	v_bfe_u32 v247, v246, 4, 1
	v_lshrrev_b32_e32 v246, 5, v246
	v_lshlrev_b32_e32 v247, 9, v247
	v_lshl_or_b32 v247, v246, 18, v247
	v_lshl_add_u32 v246, s26, 8, v1
	v_lshl_add_u32 v247, v246, 14, v247
	v_lshl_or_b32 v246, s58, 8, v224
	v_lshl_add_u32 v247, v246, 2, v247
	v_add_u32_e32 v247, s66, v247
	global_load_dword v246, v247, s[0:1]
.Ltch9_skip:
	s_and_b64 vcc, exec, s[36:37]
	s_cbranch_vccnz .LBB0_1184
	s_waitcnt vmcnt(8)
